# attention loop: K-fragment LDS reads software-pipelined one pair ahead (double-buffered in free VGPRs, counted lgkmcnt), first V transposed-read group issued before the last QK^T pair
# speedup vs baseline: 1.0003x; 1.0003x over previous
; #define LAS __attribute__((address_space(3)))
; __device__ __forceinline__ void qkt(f32x16& p0, f32x16& p1, const LAS char* Ks, const bf16x8* qr, int r32, int hi, float nm) {
; #pragma unroll
;   for (int r = 0; r < 16; ++r) { p0[r] = nm; p1[r] = nm; }
; #pragma unroll
;   for (int d0 = 0; d0 < DQK / 16; ++d0) { int cb = (d0 * 16 + hi * 8) * 2;
;     bf16x8 b0 = *reinterpret_cast<const LAS bf16x8*>(Ks + KSWZ(r32, cb));
;     bf16x8 b1 = *reinterpret_cast<const LAS bf16x8*>(Ks + KSWZ(32 + r32, cb));
;     __builtin_amdgcn_s_setprio(1);
;     p0 = __builtin_amdgcn_mfma_f32_32x32x16_bf16(b0, qr[d0], p0, 0, 0, 0);
;     p1 = __builtin_amdgcn_mfma_f32_32x32x16_bf16(b1, qr[d0], p1, 0, 0, 0);
;     __builtin_amdgcn_s_setprio(0); }
; }
; __device__ __forceinline__ int v_st(int k, int c) { const int kk = (k & ~0xC) | ((k & 4) << 1) | ((k & 8) >> 1); return ((kk >> 3) * 2 + (c >> 5)) * 512 + ((kk & 7) * 32 + (c & 31)) * 2; }
; __device__ __forceinline__ int v_rd_base(int lane) { return ((lane & 3) << 3) | (((lane >> 2) & 3) << 6) | (((lane >> 4) & 1) << 5) | (((lane >> 5) & 1) << 8); }
; template <int OFF> __device__ __forceinline__ s16x4 tr_read(int vb) {
;   s16x4 r; asm volatile("ds_read_b64_tr_b16 %0, %1 offset:%2" : "=&v"(r) : "v"(vb), "i"(OFF) : "memory"); return r;
; }
; template <int D0> __device__ __forceinline__ void pv_one(f32x16& od, int vb, bf16x8 pa0, bf16x8 pa1, bf16x8 pa2, bf16x8 pa3) {
;   const s16x4 l0 = tr_read<v_rd_off(D0, 0, 0)>(vb), h0 = tr_read<v_rd_off(D0, 0, 1)>(vb), l1 = tr_read<v_rd_off(D0, 1, 0)>(vb), h1 = tr_read<v_rd_off(D0, 1, 1)>(vb);
;   const s16x4 l2 = tr_read<v_rd_off(D0, 2, 0)>(vb), h2 = tr_read<v_rd_off(D0, 2, 1)>(vb), l3 = tr_read<v_rd_off(D0, 3, 0)>(vb), h3 = tr_read<v_rd_off(D0, 3, 1)>(vb);
;   asm volatile("s_waitcnt lgkmcnt(0)" ::: "memory"); SBAR();
;     ...
;   __builtin_amdgcn_s_setprio(1);
; __device__ __forceinline__ void attn_body(const bf16_t* __restrict__ Qb, const bf16_t* __restrict__ Kh, const bf16_t* __restrict__ Vh, unsigned char* __restrict__ Ob, int ldo, int seq, LAS char* lds, const int wv, const float kbound, const float oscale) {
;     ...
;     SBAR(); qkt(pB0, pB1, K_lds + b1 * SHM_K, qr, r32, hi, nm);
;     finishSM(pA0, pA1, l_reg, pa0, pa1, pa2, pa3); SBAR();
;     if (j + 3 < NT) SLOAD((j + 3) * KVBLK); SBAR();
;     pv_d0(o, vb0 + b0 * (int)SHM_V, pa0, pa1, pa2, pa3); partialSM(pB0, pB1);
.LBB0_605:
	v_add_u32_e32 v238, v242, v198
	ds_read_b128 v[234:237], v238 offset:24576
	ds_read_b128 v[238:241], v238 offset:32768
	v_add_u32_e32 v248, v242, v199
	ds_read_b128 v[244:247], v248 offset:24576
	ds_read_b128 v[248:251], v248 offset:32768
	v_add_f32_e32 v33, 0, v80
	v_add_f32_e32 v33, v81, v33
	v_add_f32_e32 v33, v82, v33
	v_add_f32_e32 v33, v83, v33
	v_add_f32_e32 v33, v84, v33
	v_add_f32_e32 v33, v85, v33
	s_setprio 1
	s_waitcnt lgkmcnt(3)
	v_mfma_f32_32x32x16_bf16 v[112:127], v[234:237], v[128:131], v[48:63]
	v_add_f32_e32 v33, v86, v33
	v_add_f32_e32 v33, v87, v33
	v_add_f32_e32 v33, v88, v33
	v_add_f32_e32 v33, v89, v33
	v_add_f32_e32 v33, v90, v33
	s_waitcnt lgkmcnt(2)
	v_mfma_f32_32x32x16_bf16 v[96:111], v[238:241], v[128:131], v[48:63]
	s_setprio 0
	v_add_u32_e32 v238, v242, v200
	ds_read_b128 v[234:237], v238 offset:24576
	ds_read_b128 v[238:241], v238 offset:32768
	v_add_f32_e32 v33, v91, v33
	v_exp_f32_e32 v64, v64
	v_add_f32_e32 v33, v92, v33
	v_exp_f32_e32 v65, v65
	s_setprio 1
	s_waitcnt lgkmcnt(3)
	v_mfma_f32_32x32x16_bf16 v[112:127], v[244:247], v[132:135], v[112:127]
	v_add_f32_e32 v33, v93, v33
	v_exp_f32_e32 v66, v66
	v_add_f32_e32 v33, v94, v33
	v_exp_f32_e32 v67, v67
	v_add_f32_e32 v33, v95, v33
	s_waitcnt lgkmcnt(2)
	v_mfma_f32_32x32x16_bf16 v[96:111], v[248:251], v[132:135], v[96:111]
	s_setprio 0
	v_add_u32_e32 v248, v242, v201
	ds_read_b128 v[244:247], v248 offset:24576
	ds_read_b128 v[248:251], v248 offset:32768
	v_exp_f32_e32 v68, v68
	v_add_f32_e32 v33, v64, v33
	v_exp_f32_e32 v69, v69
	v_add_f32_e32 v33, v65, v33
	s_setprio 1
	s_waitcnt lgkmcnt(3)
	v_mfma_f32_32x32x16_bf16 v[112:127], v[234:237], v[136:139], v[112:127]
	v_exp_f32_e32 v70, v70
	v_add_f32_e32 v33, v66, v33
	v_exp_f32_e32 v71, v71
	v_add_f32_e32 v33, v67, v33
	v_exp_f32_e32 v72, v72
	s_waitcnt lgkmcnt(2)
	v_mfma_f32_32x32x16_bf16 v[96:111], v[238:241], v[136:139], v[96:111]
	s_setprio 0
	v_add_u32_e32 v238, v242, v202
	ds_read_b128 v[234:237], v238 offset:24576
	ds_read_b128 v[238:241], v238 offset:32768
	v_add_f32_e32 v33, v68, v33
	v_exp_f32_e32 v73, v73
	v_add_f32_e32 v33, v69, v33
	v_exp_f32_e32 v74, v74
	s_setprio 1
	s_waitcnt lgkmcnt(3)
	v_mfma_f32_32x32x16_bf16 v[112:127], v[244:247], v[140:143], v[112:127]
	v_add_f32_e32 v33, v70, v33
	v_exp_f32_e32 v75, v75
	v_add_f32_e32 v33, v71, v33
	v_exp_f32_e32 v76, v76
	v_add_f32_e32 v33, v72, v33
	s_waitcnt lgkmcnt(2)
	v_mfma_f32_32x32x16_bf16 v[96:111], v[248:251], v[140:143], v[96:111]
	s_setprio 0
	v_add_u32_e32 v242, v242, v203
	ds_read_b128 v[244:247], v242 offset:24576
	ds_read_b128 v[248:251], v242 offset:32768
	v_exp_f32_e32 v77, v77
	v_add_f32_e32 v33, v73, v33
	v_exp_f32_e32 v78, v78
	v_add_f32_e32 v33, v74, v33
	s_setprio 1
	s_waitcnt lgkmcnt(3)
	v_mfma_f32_32x32x16_bf16 v[112:127], v[234:237], v[148:151], v[112:127]
	v_exp_f32_e32 v79, v79
	v_add_f32_e32 v33, v75, v33
	v_add_f32_e32 v33, v76, v33
	v_add_f32_e32 v33, v77, v33
	v_add_f32_e32 v33, v78, v33
	s_waitcnt lgkmcnt(2)
	v_mfma_f32_32x32x16_bf16 v[96:111], v[238:241], v[148:151], v[96:111]
	s_setprio 0
	v_add_f32_e32 v204, v79, v33
	v_mov_b32_e32 v205, v204
	v_cvt_pk_bf16_f32 v34, v80, v81
	v_cvt_pk_bf16_f32 v35, v82, v83
	s_lshl_b32 s14, s6, 13
	v_add_u32_e32 v252, s14, v188
	ds_read_b64_tr_b16 v[206:207], v252 offset:0
	ds_read_b64_tr_b16 v[208:209], v252 offset:0x400
	ds_read_b64_tr_b16 v[210:211], v252 offset:0x800
	ds_read_b64_tr_b16 v[212:213], v252 offset:0xc00
	ds_read_b64_tr_b16 v[214:215], v252 offset:0x1000
	ds_read_b64_tr_b16 v[216:217], v252 offset:0x1400
	ds_read_b64_tr_b16 v[218:219], v252 offset:0x1800
	ds_read_b64_tr_b16 v[220:221], v252 offset:0x1c00
	s_setprio 1
	s_waitcnt lgkmcnt(9)
	v_mfma_f32_32x32x16_bf16 v[112:127], v[244:247], v[144:147], v[112:127]
	v_cvt_pk_bf16_f32 v36, v84, v85
	v_cvt_pk_bf16_f32 v37, v86, v87
	v_cvt_pk_bf16_f32 v38, v88, v89
	v_cvt_pk_bf16_f32 v39, v90, v91
	v_cvt_pk_bf16_f32 v40, v92, v93
	s_waitcnt lgkmcnt(8)
	v_mfma_f32_32x32x16_bf16 v[96:111], v[248:251], v[144:147], v[96:111]
	s_setprio 0
	v_cvt_pk_bf16_f32 v41, v94, v95
	v_cvt_pk_bf16_f32 v42, v64, v65
	v_cvt_pk_bf16_f32 v43, v66, v67
	v_cvt_pk_bf16_f32 v44, v68, v69
	v_cvt_pk_bf16_f32 v45, v70, v71
	v_cvt_pk_bf16_f32 v164, v72, v73
	v_cvt_pk_bf16_f32 v165, v74, v75
	v_cvt_pk_bf16_f32 v166, v76, v77
	v_cvt_pk_bf16_f32 v167, v78, v79
	s_nop 1
	v_permlane32_swap_b32_e32 v204, v205
	v_permlane32_swap_b32_e32 v34, v36
	v_permlane32_swap_b32_e32 v35, v37
	v_permlane32_swap_b32_e32 v38, v40
	v_permlane32_swap_b32_e32 v39, v41
	v_permlane32_swap_b32_e32 v42, v44
	v_permlane32_swap_b32_e32 v43, v45
	v_permlane32_swap_b32_e32 v164, v166
	v_permlane32_swap_b32_e32 v165, v167
	s_lshl_b32 s14, s6, 13
	v_add_u32_e32 v33, s14, v188
	s_waitcnt lgkmcnt(0)
	s_setprio 1
	v_mfma_f32_32x32x16_bf16 v[0:15], v[34:37], v[206:209], v[0:15]
	v_mfma_f32_32x32x16_bf16 v[0:15], v[38:41], v[210:213], v[0:15]
	v_mfma_f32_32x32x16_bf16 v[0:15], v[42:45], v[214:217], v[0:15]
	v_mfma_f32_32x32x16_bf16 v[0:15], v[164:167], v[218:221], v[0:15]
	s_setprio 0
	ds_read_b64_tr_b16 v[206:207], v33 offset:0x200
	ds_read_b64_tr_b16 v[208:209], v33 offset:0x600
	ds_read_b64_tr_b16 v[210:211], v33 offset:0xa00
	ds_read_b64_tr_b16 v[212:213], v33 offset:0xe00
	ds_read_b64_tr_b16 v[214:215], v33 offset:0x1200
	ds_read_b64_tr_b16 v[216:217], v33 offset:0x1600
	ds_read_b64_tr_b16 v[218:219], v33 offset:0x1a00
	ds_read_b64_tr_b16 v[220:221], v33 offset:0x1e00
	s_waitcnt lgkmcnt(0)
	s_setprio 1
	v_mfma_f32_32x32x16_bf16 v[16:31], v[34:37], v[206:209], v[16:31]
	v_mfma_f32_32x32x16_bf16 v[16:31], v[38:41], v[210:213], v[16:31]
	v_mfma_f32_32x32x16_bf16 v[16:31], v[42:45], v[214:217], v[16:31]
	v_mfma_f32_32x32x16_bf16 v[16:31], v[164:167], v[218:221], v[16:31]
	s_setprio 0
	s_andn2_b64 vcc, exec, s[4:5]
	s_barrier
	s_cbranch_vccnz .LBB0_607
	s_lshl_b32 s4, s6, 14
	s_add_i32 s4, s4, 0
	v_add_u32_e32 v35, s14, v189
	v_add_u32_e32 v33, s4, v191
	v_add_u32_e32 v34, s4, v190
	s_waitcnt vmcnt(2)
	ds_write_b128 v35, v[152:155]
	s_waitcnt vmcnt(1)
	ds_write_b128 v34, v[156:159] offset:24576
	s_waitcnt vmcnt(0)
	ds_write_b128 v33, v[160:163] offset:24576

; __device__ __forceinline__ void qkt(f32x16& p0, f32x16& p1, const LAS char* Ks, const bf16x8* qr, int r32, int hi, float nm) {
; #pragma unroll
;   for (int r = 0; r < 16; ++r) { p0[r] = nm; p1[r] = nm; }
; #pragma unroll
;   for (int d0 = 0; d0 < DQK / 16; ++d0) { int cb = (d0 * 16 + hi * 8) * 2;
;     bf16x8 b0 = *reinterpret_cast<const LAS bf16x8*>(Ks + KSWZ(r32, cb));
;     bf16x8 b1 = *reinterpret_cast<const LAS bf16x8*>(Ks + KSWZ(32 + r32, cb));
;     __builtin_amdgcn_s_setprio(1);
;     p0 = __builtin_amdgcn_mfma_f32_32x32x16_bf16(b0, qr[d0], p0, 0, 0, 0);
;     p1 = __builtin_amdgcn_mfma_f32_32x32x16_bf16(b1, qr[d0], p1, 0, 0, 0);
;     __builtin_amdgcn_s_setprio(0); }
; }
; __device__ __forceinline__ int v_st(int k, int c) { const int kk = (k & ~0xC) | ((k & 4) << 1) | ((k & 8) >> 1); return ((kk >> 3) * 2 + (c >> 5)) * 512 + ((kk & 7) * 32 + (c & 31)) * 2; }
; __device__ __forceinline__ int v_rd_base(int lane) { return ((lane & 3) << 3) | (((lane >> 2) & 3) << 6) | (((lane >> 4) & 1) << 5) | (((lane >> 5) & 1) << 8); }
; template <int OFF> __device__ __forceinline__ s16x4 tr_read(int vb) {
;   s16x4 r; asm volatile("ds_read_b64_tr_b16 %0, %1 offset:%2" : "=&v"(r) : "v"(vb), "i"(OFF) : "memory"); return r;
; }
; template <int D0> __device__ __forceinline__ void pv_one(f32x16& od, int vb, bf16x8 pa0, bf16x8 pa1, bf16x8 pa2, bf16x8 pa3) {
;   const s16x4 l0 = tr_read<v_rd_off(D0, 0, 0)>(vb), h0 = tr_read<v_rd_off(D0, 0, 1)>(vb), l1 = tr_read<v_rd_off(D0, 1, 0)>(vb), h1 = tr_read<v_rd_off(D0, 1, 1)>(vb);
;   const s16x4 l2 = tr_read<v_rd_off(D0, 2, 0)>(vb), h2 = tr_read<v_rd_off(D0, 2, 1)>(vb), l3 = tr_read<v_rd_off(D0, 3, 0)>(vb), h3 = tr_read<v_rd_off(D0, 3, 1)>(vb);
;   asm volatile("s_waitcnt lgkmcnt(0)" ::: "memory"); SBAR();
;     ...
;   __builtin_amdgcn_s_setprio(1);
; __device__ __forceinline__ void attn_body(const bf16_t* __restrict__ Qb, const bf16_t* __restrict__ Kh, const bf16_t* __restrict__ Vh, unsigned char* __restrict__ Ob, int ldo, int seq, LAS char* lds, const int wv, const float kbound, const float oscale) {
;     ...
;     SBAR(); if (j + 2 < NT) qkt(pA0, pA1, K_lds + b2 * SHM_K, qr, r32, hi, nm);
;     finishSM(pB0, pB1, l_reg, pa0, pa1, pa2, pa3); SBAR();
;     if (j + 4 < NT) SLOAD((j + 4) * KVBLK); SBAR();
;     pv_d0(o, vb0 + b1 * (int)SHM_V, pa0, pa1, pa2, pa3); if (j + 2 < NT) partialSM(pA0, pA1);
.LBB0_611:
	s_cmp_lt_u32 s71, 62
	s_cselect_b64 s[14:15], -1, 0
	s_cmp_gt_u32 s71, 61
	s_cselect_b64 s[4:5], -1, 0
	s_and_b64 vcc, exec, s[4:5]
	s_cbranch_vccnz .Lattn0_s2only
	v_lshl_add_u32 v243, s72, 14, v193
	v_add_u32_e32 v238, v243, v198
	ds_read_b128 v[234:237], v238 offset:24576
	ds_read_b128 v[238:241], v238 offset:32768
	v_add_u32_e32 v248, v243, v199
	ds_read_b128 v[244:247], v248 offset:24576
	ds_read_b128 v[248:251], v248 offset:32768
	v_exp_f32_e32 v34, v112
	v_exp_f32_e32 v35, v113
	v_exp_f32_e32 v36, v114
	v_exp_f32_e32 v37, v115
	v_exp_f32_e32 v38, v116
	v_add_f32_e32 v33, 0, v34
	v_exp_f32_e32 v39, v117
	v_add_f32_e32 v33, v35, v33
	s_setprio 1
	s_waitcnt lgkmcnt(3)
	v_mfma_f32_32x32x16_bf16 v[80:95], v[234:237], v[128:131], v[48:63]
	v_exp_f32_e32 v40, v118
	v_add_f32_e32 v33, v36, v33
	v_exp_f32_e32 v41, v119
	v_add_f32_e32 v33, v37, v33
	v_exp_f32_e32 v42, v120
	v_add_f32_e32 v33, v38, v33
	s_waitcnt lgkmcnt(2)
	v_mfma_f32_32x32x16_bf16 v[64:79], v[238:241], v[128:131], v[48:63]
	s_setprio 0
	v_add_u32_e32 v238, v243, v200
	ds_read_b128 v[234:237], v238 offset:24576
	ds_read_b128 v[238:241], v238 offset:32768
	v_exp_f32_e32 v43, v121
	v_add_f32_e32 v33, v39, v33
	v_exp_f32_e32 v44, v122
	v_add_f32_e32 v33, v40, v33
	v_exp_f32_e32 v45, v123
	s_setprio 1
	s_waitcnt lgkmcnt(3)
	v_mfma_f32_32x32x16_bf16 v[80:95], v[244:247], v[132:135], v[80:95]
	v_add_f32_e32 v33, v41, v33
	v_exp_f32_e32 v47, v124
	v_add_f32_e32 v33, v42, v33
	v_exp_f32_e32 v112, v125
	v_add_f32_e32 v33, v43, v33
	v_exp_f32_e32 v113, v126
	s_waitcnt lgkmcnt(2)
	v_mfma_f32_32x32x16_bf16 v[64:79], v[248:251], v[132:135], v[64:79]
	s_setprio 0
	v_add_u32_e32 v248, v243, v201
	ds_read_b128 v[244:247], v248 offset:24576
	ds_read_b128 v[248:251], v248 offset:32768
	v_add_f32_e32 v33, v44, v33
	v_exp_f32_e32 v114, v127
	v_add_f32_e32 v33, v45, v33
	v_exp_f32_e32 v96, v96
	v_add_f32_e32 v33, v47, v33
	s_setprio 1
	s_waitcnt lgkmcnt(3)
	v_mfma_f32_32x32x16_bf16 v[80:95], v[234:237], v[136:139], v[80:95]
	v_exp_f32_e32 v97, v97
	v_add_f32_e32 v33, v112, v33
	v_exp_f32_e32 v98, v98
	v_add_f32_e32 v33, v113, v33
	v_exp_f32_e32 v99, v99
	v_add_f32_e32 v33, v114, v33
	s_waitcnt lgkmcnt(2)
	v_mfma_f32_32x32x16_bf16 v[64:79], v[238:241], v[136:139], v[64:79]
	s_setprio 0
	v_add_u32_e32 v238, v243, v202
	ds_read_b128 v[234:237], v238 offset:24576
	ds_read_b128 v[238:241], v238 offset:32768
	v_exp_f32_e32 v100, v100
	v_add_f32_e32 v33, v96, v33
	v_exp_f32_e32 v101, v101
	v_add_f32_e32 v33, v97, v33
	v_exp_f32_e32 v102, v102
	s_setprio 1
	s_waitcnt lgkmcnt(3)
	v_mfma_f32_32x32x16_bf16 v[80:95], v[244:247], v[140:143], v[80:95]
	v_add_f32_e32 v33, v98, v33
	v_exp_f32_e32 v103, v103
	v_add_f32_e32 v33, v99, v33
	v_exp_f32_e32 v104, v104
	v_add_f32_e32 v33, v100, v33
	v_exp_f32_e32 v105, v105
	s_waitcnt lgkmcnt(2)
	v_mfma_f32_32x32x16_bf16 v[64:79], v[248:251], v[140:143], v[64:79]
	s_setprio 0
	v_add_u32_e32 v248, v243, v203
	ds_read_b128 v[244:247], v248 offset:24576
	ds_read_b128 v[248:251], v248 offset:32768
	v_add_f32_e32 v33, v101, v33
	v_exp_f32_e32 v106, v106
	v_add_f32_e32 v33, v102, v33
	v_exp_f32_e32 v107, v107
	v_add_f32_e32 v33, v103, v33
	s_setprio 1
	s_waitcnt lgkmcnt(3)
	v_mfma_f32_32x32x16_bf16 v[80:95], v[234:237], v[148:151], v[80:95]
	v_exp_f32_e32 v108, v108
	v_add_f32_e32 v33, v104, v33
	v_exp_f32_e32 v109, v109
	v_add_f32_e32 v33, v105, v33
	v_exp_f32_e32 v110, v110
	v_add_f32_e32 v33, v106, v33
	s_waitcnt lgkmcnt(2)
	v_mfma_f32_32x32x16_bf16 v[64:79], v[238:241], v[148:151], v[64:79]
	s_setprio 0
	v_exp_f32_e32 v111, v111
	v_add_f32_e32 v33, v107, v33
	v_add_f32_e32 v33, v108, v33
	v_add_f32_e32 v33, v109, v33
	v_add_f32_e32 v33, v110, v33
	s_lshl_b32 s74, s70, 13
	v_add_u32_e32 v252, s74, v188
	ds_read_b64_tr_b16 v[206:207], v252 offset:0
	ds_read_b64_tr_b16 v[208:209], v252 offset:0x400
	ds_read_b64_tr_b16 v[210:211], v252 offset:0x800
	ds_read_b64_tr_b16 v[212:213], v252 offset:0xc00
	ds_read_b64_tr_b16 v[214:215], v252 offset:0x1000
	ds_read_b64_tr_b16 v[216:217], v252 offset:0x1400
	ds_read_b64_tr_b16 v[218:219], v252 offset:0x1800
	ds_read_b64_tr_b16 v[220:221], v252 offset:0x1c00
	s_setprio 1
	s_waitcnt lgkmcnt(9)
	v_mfma_f32_32x32x16_bf16 v[80:95], v[244:247], v[144:147], v[80:95]
	v_add_f32_e32 v33, v111, v33
	v_mov_b32_e32 v46, v33
	v_cvt_pk_bf16_f32 v34, v34, v35
	v_cvt_pk_bf16_f32 v35, v36, v37
	v_cvt_pk_bf16_f32 v36, v38, v39
	v_cvt_pk_bf16_f32 v37, v40, v41
	s_waitcnt lgkmcnt(8)
	v_mfma_f32_32x32x16_bf16 v[64:79], v[248:251], v[144:147], v[64:79]
	s_setprio 0
	v_cvt_pk_bf16_f32 v38, v42, v43
	v_cvt_pk_bf16_f32 v39, v44, v45
	v_cvt_pk_bf16_f32 v40, v47, v112
	v_cvt_pk_bf16_f32 v41, v113, v114
	v_cvt_pk_bf16_f32 v42, v96, v97
	v_cvt_pk_bf16_f32 v43, v98, v99
	v_cvt_pk_bf16_f32 v44, v100, v101
	v_cvt_pk_bf16_f32 v45, v102, v103
	v_cvt_pk_bf16_f32 v96, v104, v105
	v_cvt_pk_bf16_f32 v97, v106, v107
	v_cvt_pk_bf16_f32 v98, v108, v109
	v_cvt_pk_bf16_f32 v99, v110, v111
	s_nop 1
	v_permlane32_swap_b32_e32 v33, v46
	v_permlane32_swap_b32_e32 v34, v36
	v_permlane32_swap_b32_e32 v35, v37
	v_permlane32_swap_b32_e32 v38, v40
	v_permlane32_swap_b32_e32 v39, v41
	v_permlane32_swap_b32_e32 v42, v44
	v_permlane32_swap_b32_e32 v43, v45
	v_permlane32_swap_b32_e32 v96, v98
	v_permlane32_swap_b32_e32 v97, v99
	s_branch .Lattn0_join
; #define LAS __attribute__((address_space(3)))
; #define SBAR() __builtin_amdgcn_sched_barrier(0)
; __device__ __forceinline__ void finishSM(f32x16& p0, f32x16& p1, float& l_reg, bf16x8& pa0, bf16x8& pa1, bf16x8& pa2, bf16x8& pa3) {
;   for (int r = 0; r < 16; ++r) p1[r] = __builtin_amdgcn_exp2f(p1[r]);
;   float ps = 0; for (int r = 0; r < 16; ++r) ps += p0[r]; for (int r = 0; r < 16; ++r) ps += p1[r];
;   { auto rr = __builtin_amdgcn_permlane32_swap(__float_as_uint(ps), __float_as_uint(ps), false, false);
;     ps = __uint_as_float(rr[0]) + __uint_as_float(rr[1]); }
;   l_reg += ps;
;     ...
;   PK4(p0, 0, pa0); PK4(p0, 8, pa1); PK4(p1, 0, pa2); PK4(p1, 8, pa3);
;     ...
; }
; __device__ __forceinline__ void qkt(f32x16& p0, f32x16& p1, const LAS char* Ks, const bf16x8* qr, int r32, int hi, float nm) {
; #pragma unroll
;   for (int r = 0; r < 16; ++r) { p0[r] = nm; p1[r] = nm; }
; #pragma unroll
;   for (int d0 = 0; d0 < DQK / 16; ++d0) { int cb = (d0 * 16 + hi * 8) * 2;
;     bf16x8 b0 = *reinterpret_cast<const LAS bf16x8*>(Ks + KSWZ(r32, cb));
;     bf16x8 b1 = *reinterpret_cast<const LAS bf16x8*>(Ks + KSWZ(32 + r32, cb));
;     __builtin_amdgcn_s_setprio(1);
;     p0 = __builtin_amdgcn_mfma_f32_32x32x16_bf16(b0, qr[d0], p0, 0, 0, 0);
;     p1 = __builtin_amdgcn_mfma_f32_32x32x16_bf16(b1, qr[d0], p1, 0, 0, 0);
;     __builtin_amdgcn_s_setprio(0); }
; }
; __device__ __forceinline__ int v_st(int k, int c) { const int kk = (k & ~0xC) | ((k & 4) << 1) | ((k & 8) >> 1); return ((kk >> 3) * 2 + (c >> 5)) * 512 + ((kk & 7) * 32 + (c & 31)) * 2; }
; __device__ __forceinline__ int v_rd_base(int lane) { return ((lane & 3) << 3) | (((lane >> 2) & 3) << 6) | (((lane >> 4) & 1) << 5) | (((lane >> 5) & 1) << 8); }
; template <int OFF> __device__ __forceinline__ s16x4 tr_read(int vb) {
;   s16x4 r; asm volatile("ds_read_b64_tr_b16 %0, %1 offset:%2" : "=&v"(r) : "v"(vb), "i"(OFF) : "memory"); return r;
; }
; __device__ __forceinline__ void attn_body(const bf16_t* __restrict__ Qb, const bf16_t* __restrict__ Kh, const bf16_t* __restrict__ Vh, unsigned char* __restrict__ Ob, int ldo, int seq, LAS char* lds, const int wv, const float kbound, const float oscale) {
;     ...
;     finishSM(pB0, pB1, l_reg, pa0, pa1, pa2, pa3); SBAR();
;     if (j + 4 < NT) SLOAD((j + 4) * KVBLK); SBAR();
;     pv_d0(o, vb0 + b1 * (int)SHM_V, pa0, pa1, pa2, pa3); if (j + 2 < NT) partialSM(pA0, pA1);
.Lattn0_s2only:
	s_lshl_b32 s74, s70, 13
	v_add_u32_e32 v252, s74, v188
	ds_read_b64_tr_b16 v[206:207], v252 offset:0
	ds_read_b64_tr_b16 v[208:209], v252 offset:0x400
	ds_read_b64_tr_b16 v[210:211], v252 offset:0x800
	ds_read_b64_tr_b16 v[212:213], v252 offset:0xc00
	ds_read_b64_tr_b16 v[214:215], v252 offset:0x1000
	ds_read_b64_tr_b16 v[216:217], v252 offset:0x1400
	ds_read_b64_tr_b16 v[218:219], v252 offset:0x1800
	ds_read_b64_tr_b16 v[220:221], v252 offset:0x1c00
	v_exp_f32_e32 v34, v112
	v_exp_f32_e32 v35, v113
	v_exp_f32_e32 v36, v114
	v_exp_f32_e32 v37, v115
	v_exp_f32_e32 v38, v116
	v_add_f32_e32 v33, 0, v34
	v_exp_f32_e32 v39, v117
	v_add_f32_e32 v33, v35, v33
	v_exp_f32_e32 v40, v118
	v_add_f32_e32 v33, v36, v33
	v_exp_f32_e32 v41, v119
	v_add_f32_e32 v33, v37, v33
	v_exp_f32_e32 v42, v120
	v_add_f32_e32 v33, v38, v33
	v_exp_f32_e32 v43, v121
	v_add_f32_e32 v33, v39, v33
	v_exp_f32_e32 v44, v122
	v_add_f32_e32 v33, v40, v33
	v_exp_f32_e32 v45, v123
	v_add_f32_e32 v33, v41, v33
	v_exp_f32_e32 v47, v124
	v_add_f32_e32 v33, v42, v33
	v_exp_f32_e32 v112, v125
	v_add_f32_e32 v33, v43, v33
	v_exp_f32_e32 v113, v126
	v_add_f32_e32 v33, v44, v33
	v_exp_f32_e32 v114, v127
	v_add_f32_e32 v33, v45, v33
	v_exp_f32_e32 v96, v96
	v_add_f32_e32 v33, v47, v33
	v_exp_f32_e32 v97, v97
	v_add_f32_e32 v33, v112, v33
	v_exp_f32_e32 v98, v98
	v_add_f32_e32 v33, v113, v33
	v_exp_f32_e32 v99, v99
	v_add_f32_e32 v33, v114, v33
	v_exp_f32_e32 v100, v100
	v_add_f32_e32 v33, v96, v33
	v_exp_f32_e32 v101, v101
	v_add_f32_e32 v33, v97, v33
	v_exp_f32_e32 v102, v102
	v_add_f32_e32 v33, v98, v33
	v_exp_f32_e32 v103, v103
	v_add_f32_e32 v33, v99, v33
	v_exp_f32_e32 v104, v104
	v_add_f32_e32 v33, v100, v33
	v_exp_f32_e32 v105, v105
	v_add_f32_e32 v33, v101, v33
	v_exp_f32_e32 v106, v106
	v_add_f32_e32 v33, v102, v33
	v_exp_f32_e32 v107, v107
	v_add_f32_e32 v33, v103, v33
	v_exp_f32_e32 v108, v108
	v_add_f32_e32 v33, v104, v33
	v_exp_f32_e32 v109, v109
	v_add_f32_e32 v33, v105, v33
	v_exp_f32_e32 v110, v110
	v_add_f32_e32 v33, v106, v33
	v_exp_f32_e32 v111, v111
	v_add_f32_e32 v33, v107, v33
	v_add_f32_e32 v33, v108, v33
	v_add_f32_e32 v33, v109, v33
	v_add_f32_e32 v33, v110, v33
	v_add_f32_e32 v33, v111, v33
	v_mov_b32_e32 v46, v33
	v_cvt_pk_bf16_f32 v34, v34, v35
	v_cvt_pk_bf16_f32 v35, v36, v37
	v_cvt_pk_bf16_f32 v36, v38, v39
	v_cvt_pk_bf16_f32 v37, v40, v41
	v_cvt_pk_bf16_f32 v38, v42, v43
	v_cvt_pk_bf16_f32 v39, v44, v45
	v_cvt_pk_bf16_f32 v40, v47, v112
	v_cvt_pk_bf16_f32 v41, v113, v114
	v_cvt_pk_bf16_f32 v42, v96, v97
	v_cvt_pk_bf16_f32 v43, v98, v99
	v_cvt_pk_bf16_f32 v44, v100, v101
	v_cvt_pk_bf16_f32 v45, v102, v103
	v_cvt_pk_bf16_f32 v96, v104, v105
	v_cvt_pk_bf16_f32 v97, v106, v107
	v_cvt_pk_bf16_f32 v98, v108, v109
	v_cvt_pk_bf16_f32 v99, v110, v111
	s_nop 1
	v_permlane32_swap_b32_e32 v33, v46
	v_permlane32_swap_b32_e32 v34, v36
	v_permlane32_swap_b32_e32 v35, v37
	v_permlane32_swap_b32_e32 v38, v40
	v_permlane32_swap_b32_e32 v39, v41
	v_permlane32_swap_b32_e32 v42, v44
	v_permlane32_swap_b32_e32 v43, v45
	v_permlane32_swap_b32_e32 v96, v98
	v_permlane32_swap_b32_e32 v97, v99
.Lattn0_join:
	s_lshl_b32 s74, s70, 13
	v_add_u32_e32 v47, s74, v188
	s_waitcnt lgkmcnt(0)
	s_setprio 1
	v_mfma_f32_32x32x16_bf16 v[0:15], v[34:37], v[206:209], v[0:15]
	v_exp_f32_e32 v80, v80
	v_exp_f32_e32 v81, v81
	v_mfma_f32_32x32x16_bf16 v[0:15], v[38:41], v[210:213], v[0:15]
	v_exp_f32_e32 v82, v82
	v_exp_f32_e32 v83, v83
	v_mfma_f32_32x32x16_bf16 v[0:15], v[42:45], v[214:217], v[0:15]
	v_exp_f32_e32 v84, v84
	v_exp_f32_e32 v85, v85
	v_mfma_f32_32x32x16_bf16 v[0:15], v[96:99], v[218:221], v[0:15]
	v_exp_f32_e32 v86, v86
	v_exp_f32_e32 v87, v87
	s_setprio 0
	ds_read_b64_tr_b16 v[100:101], v47 offset:0x200
	ds_read_b64_tr_b16 v[102:103], v47 offset:0x600
	ds_read_b64_tr_b16 v[104:105], v47 offset:0xa00
	ds_read_b64_tr_b16 v[106:107], v47 offset:0xe00
	ds_read_b64_tr_b16 v[108:109], v47 offset:0x1200
	ds_read_b64_tr_b16 v[110:111], v47 offset:0x1600
	ds_read_b64_tr_b16 v[112:113], v47 offset:0x1a00
	ds_read_b64_tr_b16 v[114:115], v47 offset:0x1e00
	s_waitcnt lgkmcnt(0)
	s_setprio 1
	v_mfma_f32_32x32x16_bf16 v[16:31], v[34:37], v[100:103], v[16:31]
	v_exp_f32_e32 v88, v88
	v_exp_f32_e32 v89, v89
	v_mfma_f32_32x32x16_bf16 v[16:31], v[38:41], v[104:107], v[16:31]
	v_exp_f32_e32 v90, v90
	v_exp_f32_e32 v91, v91
	v_mfma_f32_32x32x16_bf16 v[16:31], v[42:45], v[108:111], v[16:31]
	v_exp_f32_e32 v92, v92
	v_exp_f32_e32 v93, v93
	v_mfma_f32_32x32x16_bf16 v[16:31], v[96:99], v[112:115], v[16:31]
	v_exp_f32_e32 v94, v94
	v_exp_f32_e32 v95, v95
	s_setprio 0

; __device__ __forceinline__ void qkt(f32x16& p0, f32x16& p1, const LAS char* Ks, const bf16x8* qr, int r32, int hi, float nm) {
; #pragma unroll
;   for (int r = 0; r < 16; ++r) { p0[r] = nm; p1[r] = nm; }
; #pragma unroll
;   for (int d0 = 0; d0 < DQK / 16; ++d0) { int cb = (d0 * 16 + hi * 8) * 2;
;     bf16x8 b0 = *reinterpret_cast<const LAS bf16x8*>(Ks + KSWZ(r32, cb));
;     bf16x8 b1 = *reinterpret_cast<const LAS bf16x8*>(Ks + KSWZ(32 + r32, cb));
;     __builtin_amdgcn_s_setprio(1);
;     p0 = __builtin_amdgcn_mfma_f32_32x32x16_bf16(b0, qr[d0], p0, 0, 0, 0);
;     p1 = __builtin_amdgcn_mfma_f32_32x32x16_bf16(b1, qr[d0], p1, 0, 0, 0);
;     __builtin_amdgcn_s_setprio(0); }
; }
; __device__ __forceinline__ int v_st(int k, int c) { const int kk = (k & ~0xC) | ((k & 4) << 1) | ((k & 8) >> 1); return ((kk >> 3) * 2 + (c >> 5)) * 512 + ((kk & 7) * 32 + (c & 31)) * 2; }
; __device__ __forceinline__ int v_rd_base(int lane) { return ((lane & 3) << 3) | (((lane >> 2) & 3) << 6) | (((lane >> 4) & 1) << 5) | (((lane >> 5) & 1) << 8); }
; template <int OFF> __device__ __forceinline__ s16x4 tr_read(int vb) {
;   s16x4 r; asm volatile("ds_read_b64_tr_b16 %0, %1 offset:%2" : "=&v"(r) : "v"(vb), "i"(OFF) : "memory"); return r;
; }
; template <int D0> __device__ __forceinline__ void pv_one(f32x16& od, int vb, bf16x8 pa0, bf16x8 pa1, bf16x8 pa2, bf16x8 pa3) {
;   const s16x4 l0 = tr_read<v_rd_off(D0, 0, 0)>(vb), h0 = tr_read<v_rd_off(D0, 0, 1)>(vb), l1 = tr_read<v_rd_off(D0, 1, 0)>(vb), h1 = tr_read<v_rd_off(D0, 1, 1)>(vb);
;   const s16x4 l2 = tr_read<v_rd_off(D0, 2, 0)>(vb), h2 = tr_read<v_rd_off(D0, 2, 1)>(vb), l3 = tr_read<v_rd_off(D0, 3, 0)>(vb), h3 = tr_read<v_rd_off(D0, 3, 1)>(vb);
;   asm volatile("s_waitcnt lgkmcnt(0)" ::: "memory"); SBAR();
;     ...
;   __builtin_amdgcn_s_setprio(1);
; __device__ __forceinline__ void attn_body(const bf16_t* __restrict__ Qb, const bf16_t* __restrict__ Kh, const bf16_t* __restrict__ Vh, unsigned char* __restrict__ Ob, int ldo, int seq, LAS char* lds, const int wv, const float kbound, const float oscale) {
;     ...
;     SBAR(); if (j + 2 < NT) qkt(pA0, pA1, K_lds + b2 * SHM_K, qr, r32, hi, nm);
;     finishSM(pB0, pB1, l_reg, pa0, pa1, pa2, pa3); SBAR();
;     if (j + 4 < NT) SLOAD((j + 4) * KVBLK); SBAR();
;     pv_d0(o, vb0 + b1 * (int)SHM_V, pa0, pa1, pa2, pa3); if (j + 2 < NT) partialSM(pA0, pA1);
.LBB0_3152:
	s_cmp_lt_u32 s73, 62
	s_cselect_b64 s[14:15], -1, 0
	s_cmp_gt_u32 s73, 61
	s_cselect_b64 s[4:5], -1, 0
	s_and_b64 vcc, exec, s[4:5]
	s_cbranch_vccnz .Lattn1_s2only
	v_lshl_add_u32 v243, s74, 14, v193
	v_add_u32_e32 v238, v243, v198
	ds_read_b128 v[234:237], v238 offset:24576
	ds_read_b128 v[238:241], v238 offset:32768
	v_add_u32_e32 v248, v243, v199
	ds_read_b128 v[244:247], v248 offset:24576
	ds_read_b128 v[248:251], v248 offset:32768
	v_exp_f32_e32 v34, v112
	v_exp_f32_e32 v35, v113
	v_exp_f32_e32 v36, v114
	v_exp_f32_e32 v37, v115
	v_exp_f32_e32 v38, v116
	v_add_f32_e32 v33, 0, v34
	v_exp_f32_e32 v39, v117
	v_add_f32_e32 v33, v35, v33
	s_setprio 1
	s_waitcnt lgkmcnt(3)
	v_mfma_f32_32x32x16_bf16 v[80:95], v[234:237], v[128:131], v[48:63]
	v_exp_f32_e32 v40, v118
	v_add_f32_e32 v33, v36, v33
	v_exp_f32_e32 v41, v119
	v_add_f32_e32 v33, v37, v33
	v_exp_f32_e32 v42, v120
	v_add_f32_e32 v33, v38, v33
	s_waitcnt lgkmcnt(2)
	v_mfma_f32_32x32x16_bf16 v[64:79], v[238:241], v[128:131], v[48:63]
	s_setprio 0
	v_add_u32_e32 v238, v243, v200
	ds_read_b128 v[234:237], v238 offset:24576
	ds_read_b128 v[238:241], v238 offset:32768
	v_exp_f32_e32 v43, v121
	v_add_f32_e32 v33, v39, v33
	v_exp_f32_e32 v44, v122
	v_add_f32_e32 v33, v40, v33
	v_exp_f32_e32 v45, v123
	s_setprio 1
	s_waitcnt lgkmcnt(3)
	v_mfma_f32_32x32x16_bf16 v[80:95], v[244:247], v[132:135], v[80:95]
	v_add_f32_e32 v33, v41, v33
	v_exp_f32_e32 v47, v124
	v_add_f32_e32 v33, v42, v33
	v_exp_f32_e32 v112, v125
	v_add_f32_e32 v33, v43, v33
	v_exp_f32_e32 v113, v126
	s_waitcnt lgkmcnt(2)
	v_mfma_f32_32x32x16_bf16 v[64:79], v[248:251], v[132:135], v[64:79]
	s_setprio 0
	v_add_u32_e32 v248, v243, v201
	ds_read_b128 v[244:247], v248 offset:24576
	ds_read_b128 v[248:251], v248 offset:32768
	v_add_f32_e32 v33, v44, v33
	v_exp_f32_e32 v114, v127
	v_add_f32_e32 v33, v45, v33
	v_exp_f32_e32 v96, v96
	v_add_f32_e32 v33, v47, v33
	s_setprio 1
	s_waitcnt lgkmcnt(3)
	v_mfma_f32_32x32x16_bf16 v[80:95], v[234:237], v[136:139], v[80:95]
	v_exp_f32_e32 v97, v97
	v_add_f32_e32 v33, v112, v33
	v_exp_f32_e32 v98, v98
	v_add_f32_e32 v33, v113, v33
	v_exp_f32_e32 v99, v99
	v_add_f32_e32 v33, v114, v33
	s_waitcnt lgkmcnt(2)
	v_mfma_f32_32x32x16_bf16 v[64:79], v[238:241], v[136:139], v[64:79]
	s_setprio 0
	v_add_u32_e32 v238, v243, v202
	ds_read_b128 v[234:237], v238 offset:24576
	ds_read_b128 v[238:241], v238 offset:32768
	v_exp_f32_e32 v100, v100
	v_add_f32_e32 v33, v96, v33
	v_exp_f32_e32 v101, v101
	v_add_f32_e32 v33, v97, v33
	v_exp_f32_e32 v102, v102
	s_setprio 1
	s_waitcnt lgkmcnt(3)
	v_mfma_f32_32x32x16_bf16 v[80:95], v[244:247], v[140:143], v[80:95]
	v_add_f32_e32 v33, v98, v33
	v_exp_f32_e32 v103, v103
	v_add_f32_e32 v33, v99, v33
	v_exp_f32_e32 v104, v104
	v_add_f32_e32 v33, v100, v33
	v_exp_f32_e32 v105, v105
	s_waitcnt lgkmcnt(2)
	v_mfma_f32_32x32x16_bf16 v[64:79], v[248:251], v[140:143], v[64:79]
	s_setprio 0
	v_add_u32_e32 v248, v243, v203
	ds_read_b128 v[244:247], v248 offset:24576
	ds_read_b128 v[248:251], v248 offset:32768
	v_add_f32_e32 v33, v101, v33
	v_exp_f32_e32 v106, v106
	v_add_f32_e32 v33, v102, v33
	v_exp_f32_e32 v107, v107
	v_add_f32_e32 v33, v103, v33
	s_setprio 1
	s_waitcnt lgkmcnt(3)
	v_mfma_f32_32x32x16_bf16 v[80:95], v[234:237], v[148:151], v[80:95]
	v_exp_f32_e32 v108, v108
	v_add_f32_e32 v33, v104, v33
	v_exp_f32_e32 v109, v109
	v_add_f32_e32 v33, v105, v33
	v_exp_f32_e32 v110, v110
	v_add_f32_e32 v33, v106, v33
	s_waitcnt lgkmcnt(2)
	v_mfma_f32_32x32x16_bf16 v[64:79], v[238:241], v[148:151], v[64:79]
	s_setprio 0
	v_exp_f32_e32 v111, v111
	v_add_f32_e32 v33, v107, v33
	v_add_f32_e32 v33, v108, v33
	v_add_f32_e32 v33, v109, v33
	v_add_f32_e32 v33, v110, v33
	s_lshl_b32 s76, s72, 13
	v_add_u32_e32 v252, s76, v188
	ds_read_b64_tr_b16 v[206:207], v252 offset:0
	ds_read_b64_tr_b16 v[208:209], v252 offset:0x400
	ds_read_b64_tr_b16 v[210:211], v252 offset:0x800
	ds_read_b64_tr_b16 v[212:213], v252 offset:0xc00
	ds_read_b64_tr_b16 v[214:215], v252 offset:0x1000
	ds_read_b64_tr_b16 v[216:217], v252 offset:0x1400
	ds_read_b64_tr_b16 v[218:219], v252 offset:0x1800
	ds_read_b64_tr_b16 v[220:221], v252 offset:0x1c00
	s_setprio 1
	s_waitcnt lgkmcnt(9)
	v_mfma_f32_32x32x16_bf16 v[80:95], v[244:247], v[144:147], v[80:95]
	v_add_f32_e32 v33, v111, v33
	v_mov_b32_e32 v46, v33
	v_cvt_pk_bf16_f32 v34, v34, v35
	v_cvt_pk_bf16_f32 v35, v36, v37
	v_cvt_pk_bf16_f32 v36, v38, v39
	v_cvt_pk_bf16_f32 v37, v40, v41
	s_waitcnt lgkmcnt(8)
	v_mfma_f32_32x32x16_bf16 v[64:79], v[248:251], v[144:147], v[64:79]
	s_setprio 0
	v_cvt_pk_bf16_f32 v38, v42, v43
	v_cvt_pk_bf16_f32 v39, v44, v45
	v_cvt_pk_bf16_f32 v40, v47, v112
	v_cvt_pk_bf16_f32 v41, v113, v114
	v_cvt_pk_bf16_f32 v42, v96, v97
	v_cvt_pk_bf16_f32 v43, v98, v99
	v_cvt_pk_bf16_f32 v44, v100, v101
	v_cvt_pk_bf16_f32 v45, v102, v103
	v_cvt_pk_bf16_f32 v96, v104, v105
	v_cvt_pk_bf16_f32 v97, v106, v107
	v_cvt_pk_bf16_f32 v98, v108, v109
	v_cvt_pk_bf16_f32 v99, v110, v111
	s_nop 1
	v_permlane32_swap_b32_e32 v33, v46
	v_permlane32_swap_b32_e32 v34, v36
	v_permlane32_swap_b32_e32 v35, v37
	v_permlane32_swap_b32_e32 v38, v40
	v_permlane32_swap_b32_e32 v39, v41
	v_permlane32_swap_b32_e32 v42, v44
	v_permlane32_swap_b32_e32 v43, v45
	v_permlane32_swap_b32_e32 v96, v98
	v_permlane32_swap_b32_e32 v97, v99
	s_branch .Lattn1_join
; #define LAS __attribute__((address_space(3)))
; #define SBAR() __builtin_amdgcn_sched_barrier(0)
; __device__ __forceinline__ void finishSM(f32x16& p0, f32x16& p1, float& l_reg, bf16x8& pa0, bf16x8& pa1, bf16x8& pa2, bf16x8& pa3) {
;   for (int r = 0; r < 16; ++r) p1[r] = __builtin_amdgcn_exp2f(p1[r]);
;   float ps = 0; for (int r = 0; r < 16; ++r) ps += p0[r]; for (int r = 0; r < 16; ++r) ps += p1[r];
;   { auto rr = __builtin_amdgcn_permlane32_swap(__float_as_uint(ps), __float_as_uint(ps), false, false);
;     ps = __uint_as_float(rr[0]) + __uint_as_float(rr[1]); }
;   l_reg += ps;
;     ...
;   PK4(p0, 0, pa0); PK4(p0, 8, pa1); PK4(p1, 0, pa2); PK4(p1, 8, pa3);
;     ...
; }
; __device__ __forceinline__ void qkt(f32x16& p0, f32x16& p1, const LAS char* Ks, const bf16x8* qr, int r32, int hi, float nm) {
; #pragma unroll
;   for (int r = 0; r < 16; ++r) { p0[r] = nm; p1[r] = nm; }
; #pragma unroll
;   for (int d0 = 0; d0 < DQK / 16; ++d0) { int cb = (d0 * 16 + hi * 8) * 2;
;     bf16x8 b0 = *reinterpret_cast<const LAS bf16x8*>(Ks + KSWZ(r32, cb));
;     bf16x8 b1 = *reinterpret_cast<const LAS bf16x8*>(Ks + KSWZ(32 + r32, cb));
;     __builtin_amdgcn_s_setprio(1);
;     p0 = __builtin_amdgcn_mfma_f32_32x32x16_bf16(b0, qr[d0], p0, 0, 0, 0);
;     p1 = __builtin_amdgcn_mfma_f32_32x32x16_bf16(b1, qr[d0], p1, 0, 0, 0);
;     __builtin_amdgcn_s_setprio(0); }
; }
; __device__ __forceinline__ int v_st(int k, int c) { const int kk = (k & ~0xC) | ((k & 4) << 1) | ((k & 8) >> 1); return ((kk >> 3) * 2 + (c >> 5)) * 512 + ((kk & 7) * 32 + (c & 31)) * 2; }
; __device__ __forceinline__ int v_rd_base(int lane) { return ((lane & 3) << 3) | (((lane >> 2) & 3) << 6) | (((lane >> 4) & 1) << 5) | (((lane >> 5) & 1) << 8); }
; template <int OFF> __device__ __forceinline__ s16x4 tr_read(int vb) {
;   s16x4 r; asm volatile("ds_read_b64_tr_b16 %0, %1 offset:%2" : "=&v"(r) : "v"(vb), "i"(OFF) : "memory"); return r;
; }
; __device__ __forceinline__ void attn_body(const bf16_t* __restrict__ Qb, const bf16_t* __restrict__ Kh, const bf16_t* __restrict__ Vh, unsigned char* __restrict__ Ob, int ldo, int seq, LAS char* lds, const int wv, const float kbound, const float oscale) {
;     ...
;     finishSM(pB0, pB1, l_reg, pa0, pa1, pa2, pa3); SBAR();
;     if (j + 4 < NT) SLOAD((j + 4) * KVBLK); SBAR();
;     pv_d0(o, vb0 + b1 * (int)SHM_V, pa0, pa1, pa2, pa3); if (j + 2 < NT) partialSM(pA0, pA1);
.Lattn1_s2only:
	s_lshl_b32 s76, s72, 13
	v_add_u32_e32 v252, s76, v188
	ds_read_b64_tr_b16 v[206:207], v252 offset:0
	ds_read_b64_tr_b16 v[208:209], v252 offset:0x400
	ds_read_b64_tr_b16 v[210:211], v252 offset:0x800
	ds_read_b64_tr_b16 v[212:213], v252 offset:0xc00
	ds_read_b64_tr_b16 v[214:215], v252 offset:0x1000
	ds_read_b64_tr_b16 v[216:217], v252 offset:0x1400
	ds_read_b64_tr_b16 v[218:219], v252 offset:0x1800
	ds_read_b64_tr_b16 v[220:221], v252 offset:0x1c00
	v_exp_f32_e32 v34, v112
	v_exp_f32_e32 v35, v113
	v_exp_f32_e32 v36, v114
	v_exp_f32_e32 v37, v115
	v_exp_f32_e32 v38, v116
	v_add_f32_e32 v33, 0, v34
	v_exp_f32_e32 v39, v117
	v_add_f32_e32 v33, v35, v33
	v_exp_f32_e32 v40, v118
	v_add_f32_e32 v33, v36, v33
	v_exp_f32_e32 v41, v119
	v_add_f32_e32 v33, v37, v33
	v_exp_f32_e32 v42, v120
	v_add_f32_e32 v33, v38, v33
	v_exp_f32_e32 v43, v121
	v_add_f32_e32 v33, v39, v33
	v_exp_f32_e32 v44, v122
	v_add_f32_e32 v33, v40, v33
	v_exp_f32_e32 v45, v123
	v_add_f32_e32 v33, v41, v33
	v_exp_f32_e32 v47, v124
	v_add_f32_e32 v33, v42, v33
	v_exp_f32_e32 v112, v125
	v_add_f32_e32 v33, v43, v33
	v_exp_f32_e32 v113, v126
	v_add_f32_e32 v33, v44, v33
	v_exp_f32_e32 v114, v127
	v_add_f32_e32 v33, v45, v33
	v_exp_f32_e32 v96, v96
	v_add_f32_e32 v33, v47, v33
	v_exp_f32_e32 v97, v97
	v_add_f32_e32 v33, v112, v33
	v_exp_f32_e32 v98, v98
	v_add_f32_e32 v33, v113, v33
	v_exp_f32_e32 v99, v99
	v_add_f32_e32 v33, v114, v33
	v_exp_f32_e32 v100, v100
	v_add_f32_e32 v33, v96, v33
	v_exp_f32_e32 v101, v101
	v_add_f32_e32 v33, v97, v33
	v_exp_f32_e32 v102, v102
	v_add_f32_e32 v33, v98, v33
	v_exp_f32_e32 v103, v103
	v_add_f32_e32 v33, v99, v33
	v_exp_f32_e32 v104, v104
	v_add_f32_e32 v33, v100, v33
	v_exp_f32_e32 v105, v105
	v_add_f32_e32 v33, v101, v33
	v_exp_f32_e32 v106, v106
	v_add_f32_e32 v33, v102, v33
	v_exp_f32_e32 v107, v107
	v_add_f32_e32 v33, v103, v33
	v_exp_f32_e32 v108, v108
	v_add_f32_e32 v33, v104, v33
	v_exp_f32_e32 v109, v109
	v_add_f32_e32 v33, v105, v33
	v_exp_f32_e32 v110, v110
	v_add_f32_e32 v33, v106, v33
	v_exp_f32_e32 v111, v111
	v_add_f32_e32 v33, v107, v33
	v_add_f32_e32 v33, v108, v33
	v_add_f32_e32 v33, v109, v33
	v_add_f32_e32 v33, v110, v33
	v_add_f32_e32 v33, v111, v33
	v_mov_b32_e32 v46, v33
	v_cvt_pk_bf16_f32 v34, v34, v35
	v_cvt_pk_bf16_f32 v35, v36, v37
	v_cvt_pk_bf16_f32 v36, v38, v39
	v_cvt_pk_bf16_f32 v37, v40, v41
	v_cvt_pk_bf16_f32 v38, v42, v43
	v_cvt_pk_bf16_f32 v39, v44, v45
	v_cvt_pk_bf16_f32 v40, v47, v112
	v_cvt_pk_bf16_f32 v41, v113, v114
	v_cvt_pk_bf16_f32 v42, v96, v97
	v_cvt_pk_bf16_f32 v43, v98, v99
	v_cvt_pk_bf16_f32 v44, v100, v101
	v_cvt_pk_bf16_f32 v45, v102, v103
	v_cvt_pk_bf16_f32 v96, v104, v105
	v_cvt_pk_bf16_f32 v97, v106, v107
	v_cvt_pk_bf16_f32 v98, v108, v109
	v_cvt_pk_bf16_f32 v99, v110, v111
	s_nop 1
	v_permlane32_swap_b32_e32 v33, v46
	v_permlane32_swap_b32_e32 v34, v36
	v_permlane32_swap_b32_e32 v35, v37
	v_permlane32_swap_b32_e32 v38, v40
	v_permlane32_swap_b32_e32 v39, v41
	v_permlane32_swap_b32_e32 v42, v44
	v_permlane32_swap_b32_e32 v43, v45
	v_permlane32_swap_b32_e32 v96, v98
	v_permlane32_swap_b32_e32 v97, v99
.Lattn1_join:
	s_lshl_b32 s76, s72, 13
	v_add_u32_e32 v47, s76, v188
	s_waitcnt lgkmcnt(0)
	s_setprio 1
	v_mfma_f32_32x32x16_bf16 v[0:15], v[34:37], v[206:209], v[0:15]
	v_exp_f32_e32 v80, v80
	v_exp_f32_e32 v81, v81
	v_mfma_f32_32x32x16_bf16 v[0:15], v[38:41], v[210:213], v[0:15]
	v_exp_f32_e32 v82, v82
	v_exp_f32_e32 v83, v83
	v_mfma_f32_32x32x16_bf16 v[0:15], v[42:45], v[214:217], v[0:15]
	v_exp_f32_e32 v84, v84
	v_exp_f32_e32 v85, v85
	v_mfma_f32_32x32x16_bf16 v[0:15], v[96:99], v[218:221], v[0:15]
	v_exp_f32_e32 v86, v86
	v_exp_f32_e32 v87, v87
	s_setprio 0
	ds_read_b64_tr_b16 v[100:101], v47 offset:0x200
	ds_read_b64_tr_b16 v[102:103], v47 offset:0x600
	ds_read_b64_tr_b16 v[104:105], v47 offset:0xa00
	ds_read_b64_tr_b16 v[106:107], v47 offset:0xe00
	ds_read_b64_tr_b16 v[108:109], v47 offset:0x1200
	ds_read_b64_tr_b16 v[110:111], v47 offset:0x1600
	ds_read_b64_tr_b16 v[112:113], v47 offset:0x1a00
	ds_read_b64_tr_b16 v[114:115], v47 offset:0x1e00
	s_waitcnt lgkmcnt(0)
	s_setprio 1
	v_mfma_f32_32x32x16_bf16 v[16:31], v[34:37], v[100:103], v[16:31]
	v_exp_f32_e32 v88, v88
	v_exp_f32_e32 v89, v89
	v_mfma_f32_32x32x16_bf16 v[16:31], v[38:41], v[104:107], v[16:31]
	v_exp_f32_e32 v90, v90
	v_exp_f32_e32 v91, v91
	v_mfma_f32_32x32x16_bf16 v[16:31], v[42:45], v[108:111], v[16:31]
	v_exp_f32_e32 v92, v92
	v_exp_f32_e32 v93, v93
	v_mfma_f32_32x32x16_bf16 v[16:31], v[96:99], v[112:115], v[16:31]
	v_exp_f32_e32 v94, v94
	v_exp_f32_e32 v95, v95
	s_setprio 0
